# agg1: row-start table permuted by rank together with the keys, so the rank-group fetch is one LDS round trip instead of two dependent ones
# speedup vs baseline: 1.0036x; 1.0036x over previous
_Z11agg1_kernelPKDF16_PKfS2_PKiS4_S2_S2_PDF16_PfS6_i:
	s_load_dwordx8 s[4:11], s[0:1], 0x0
	s_load_dwordx8 s[12:19], s[0:1], 0x20
	s_load_dwordx4 s[20:23], s[0:1], 0x40
	s_load_dword s24, s[0:1], 0x50
	v_lshlrev_b32_e32 v32, 2, v0
	v_readfirstlane_b32 s25, v0
	s_lshl_b32 s26, s2, 5
	v_and_b32_e32 v64, 7, v0
	v_bfe_u32 v65, v0, 3, 3
	v_and_b32_e32 v45, 31, v0
	s_lshr_b32 s25, s25, 6
	s_getreg_b32 s30, hwreg(HW_REG_HW_ID, 4, 2)
	s_lshr_b32 s31, s2, 8
	s_lshl_b32 s31, s31, 3
	s_mov_b32 s44, 0x276c9c8d
	s_mov_b32 s45, 0xe46393
	s_and_b32 s47, s2, 0xff
	s_cmp_lt_u32 s47, 27
	s_cselect_b32 s44, 0xb1784b63, s44
	s_cselect_b32 s45, 0x1e4ee4, s45
	s_lshr_b64 s[44:45], s[44:45], s31
	s_lshl_b32 s31, s30, 1
	s_lshr_b32 s44, s44, s31
	s_and_b32 s44, s44, 3
	s_lshl_b32 s45, 1, s30
	s_lshl_b32 s46, s25, 2
	s_addk_i32 s46, 0x2800
	v_mov_b32_e32 v49, s45
	v_mov_b32_e32 v50, s46
	ds_write_b32 v50, v49
	v_lshlrev_b32_e32 v1, 1, v64
	v_add_u32_e32 v46, s26, v45
	s_waitcnt lgkmcnt(0)
	global_load_dword v33, v32, s[14:15]
	global_load_dword v34, v32, s[16:17]
	s_add_i32 s28, s24, -1
	v_cmp_gt_i32_e64 s[38:39], s24, v46
	v_min_i32_e32 v46, s28, v46
	v_lshlrev_b32_e32 v47, 2, v46
	global_load_dword v44, v47, s[10:11]
	global_load_dword v48, v47, s[10:11] offset:4
	s_lshl_b32 s27, s25, 11
	v_lshlrev_b32_e32 v62, 6, v64
	v_add_u32_e32 v62, 0x2000, v62
	v_cmp_eq_u32_e64 s[34:35], 0, v64
	v_lshlrev_b32_e32 v35, 8, v64
	v_lshl_add_u32 v35, v65, 4, v35
	v_add_u32_e32 v63, s27, v35
	v_mov_b32_e32 v36, 0
	v_mov_b32_e32 v37, 0
	v_mov_b32_e32 v38, 0
	v_mov_b32_e32 v39, 0
	s_waitcnt vmcnt(2)
	ds_write2st64_b32 v32, v33, v34 offset0:32 offset1:36
	ds_write_b128 v63, v[36:39]
	ds_write_b128 v63, v[36:39] offset:128
	s_waitcnt vmcnt(0)
	v_sub_u32_e32 v48, v48, v44
	v_add_u32_e32 v48, 1, v48
	v_cndmask_b32_e64 v48, 0, v48, s[38:39]
	v_lshl_or_b32 v40, v48, 5, v45
	s_lshl_b32 s31, s25, 2
	s_addk_i32 s31, 0x2810
	s_lshl_b32 s47, s25, 3
	v_mov_b32_e32 v41, 0
	s_nop 1
	v_readlane_b32 s46, v40, s47
	s_add_i32 s47, s47, 1
	v_cmp_gt_u32_e32 vcc, s46, v40
	v_addc_co_u32_e32 v41, vcc, 0, v41, vcc
	v_readlane_b32 s46, v40, s47
	s_add_i32 s47, s47, 1
	v_cmp_gt_u32_e32 vcc, s46, v40
	v_addc_co_u32_e32 v41, vcc, 0, v41, vcc
	v_readlane_b32 s46, v40, s47
	s_add_i32 s47, s47, 1
	v_cmp_gt_u32_e32 vcc, s46, v40
	v_addc_co_u32_e32 v41, vcc, 0, v41, vcc
	v_readlane_b32 s46, v40, s47
	s_add_i32 s47, s47, 1
	v_cmp_gt_u32_e32 vcc, s46, v40
	v_addc_co_u32_e32 v41, vcc, 0, v41, vcc
	v_readlane_b32 s46, v40, s47
	s_add_i32 s47, s47, 1
	v_cmp_gt_u32_e32 vcc, s46, v40
	v_addc_co_u32_e32 v41, vcc, 0, v41, vcc
	v_readlane_b32 s46, v40, s47
	s_add_i32 s47, s47, 1
	v_cmp_gt_u32_e32 vcc, s46, v40
	v_addc_co_u32_e32 v41, vcc, 0, v41, vcc
	v_readlane_b32 s46, v40, s47
	s_add_i32 s47, s47, 1
	v_cmp_gt_u32_e32 vcc, s46, v40
	v_addc_co_u32_e32 v41, vcc, 0, v41, vcc
	v_readlane_b32 s46, v40, s47
	s_add_i32 s47, s47, 1
	v_cmp_gt_u32_e32 vcc, s46, v40
	v_addc_co_u32_e32 v41, vcc, 0, v41, vcc
	v_lshl_add_u32 v42, v45, 4, s31
	ds_write_b32 v42, v41
	v_mov_b32_e32 v50, 0x2800
	s_waitcnt lgkmcnt(0)
	s_barrier
	ds_read_b128 v[52:55], v50
	v_lshlrev_b32_e32 v42, 4, v45
	ds_read_b128 v[48:51], v42 offset:10256
	s_waitcnt lgkmcnt(1)
	v_or3_b32 v52, v52, v53, v54
	v_or_b32_e32 v52, v52, v55
	s_nop 0
	v_readfirstlane_b32 s46, v52
	s_cmp_eq_u32 s46, 15
	s_cselect_b32 s44, s44, s25
	s_lshl_b32 s40, s44, 3
	s_waitcnt lgkmcnt(0)
	v_add3_u32 v48, v48, v49, v50
	v_add_u32_e32 v48, v48, v51
	v_lshlrev_b32_e32 v48, 2, v48
	ds_permute_b32 v40, v48, v40
	ds_permute_b32 v41, v48, v44
	v_add_u32_e32 v45, s40, v65
	v_lshlrev_b32_e32 v45, 2, v45
	s_waitcnt lgkmcnt(0)
	ds_bpermute_b32 v46, v45, v40
	ds_bpermute_b32 v10, v45, v41
	s_waitcnt lgkmcnt(1)
	v_and_b32_e32 v15, 31, v46
	v_lshrrev_b32_e32 v11, 5, v46
	v_add_u32_e32 v66, s26, v15
	v_min_i32_e32 v66, s28, v66
	v_cmp_lt_u32_e64 s[36:37], 0, v11
	v_lshlrev_b32_e32 v4, 2, v66
	v_lshlrev_b32_e32 v35, 2, v64
	v_lshl_or_b32 v35, v66, 5, v35
	global_load_dword v9, v35, s[8:9]
	v_lshrrev_b32_e32 v3, 3, v15
	v_lshlrev_b32_e32 v3, 11, v3
	v_and_b32_e32 v47, 7, v15
	v_lshl_add_u32 v3, v47, 1, v3
	v_lshl_add_u32 v3, v64, 4, v3
	v_readfirstlane_b32 s29, v11
	s_waitcnt lgkmcnt(0)
	v_add_u32_e32 v67, v10, v64
	v_lshlrev_b32_e32 v67, 2, v67
	v_mov_b32_e32 v5, s24
	v_mov_b32_e32 v6, s24
	v_mov_b32_e32 v7, s24
	v_mov_b32_e32 v8, s24
	v_mov_b32_e32 v69, s24
	v_cndmask_b32_e64 v5, v5, v66, s[34:35]
	v_cmp_gt_i32_e32 vcc, v11, v64
	s_andn2_b64 s[40:41], vcc, s[34:35]
	s_and_saveexec_b64 s[32:33], s[40:41]
	global_load_dword v5, v67, s[12:13] offset:-4
	s_mov_b64 exec, s[32:33]
	v_add_u32_e32 v68, 8, v64
	v_cmp_gt_i32_e32 vcc, v11, v68
	s_and_saveexec_b64 s[32:33], vcc
	global_load_dword v6, v67, s[12:13] offset:28
	s_mov_b64 exec, s[32:33]
	v_add_u32_e32 v68, 16, v64
	v_cmp_gt_i32_e32 vcc, v11, v68
	s_and_saveexec_b64 s[32:33], vcc
	global_load_dword v7, v67, s[12:13] offset:60
	s_mov_b64 exec, s[32:33]
	v_add_u32_e32 v68, 24, v64
	v_cmp_gt_i32_e32 vcc, v11, v68
	s_and_saveexec_b64 s[32:33], vcc
	global_load_dword v8, v67, s[12:13] offset:92
	s_mov_b64 exec, s[32:33]
	v_add_u32_e32 v68, 32, v64
	v_cmp_gt_i32_e32 vcc, v11, v68
	s_and_saveexec_b64 s[32:33], vcc
	global_load_dword v69, v67, s[12:13] offset:124
	s_mov_b64 exec, s[32:33]
	s_waitcnt vmcnt(0)
	v_lshlrev_b32_e32 v5, 4, v5
	v_lshlrev_b32_e32 v6, 4, v6
	v_lshlrev_b32_e32 v7, 4, v7
	v_lshlrev_b32_e32 v8, 4, v8
	v_lshlrev_b32_e32 v69, 4, v69
	s_mov_b32 s42, 0
	s_mov_b32 s43, 0
	ds_swizzle_b32 v32, v5 offset:swizzle(BITMASK_PERM, "pp000")
	ds_swizzle_b32 v33, v5 offset:swizzle(BITMASK_PERM, "pp001")
	ds_swizzle_b32 v34, v5 offset:swizzle(BITMASK_PERM, "pp010")
	ds_swizzle_b32 v35, v5 offset:swizzle(BITMASK_PERM, "pp011")
	s_cmp_lt_i32 s29, 3
	s_cbranch_scc1 .Lagg_first_half
	s_waitcnt lgkmcnt(0)
	v_or_b32_e32 v32, v32, v1
	v_or_b32_e32 v33, v33, v1
	v_or_b32_e32 v34, v34, v1
	v_or_b32_e32 v35, v35, v1
	global_load_ushort v36, v32, s[6:7]
	global_load_ushort v37, v33, s[6:7]
	global_load_ushort v38, v34, s[6:7]
	global_load_ushort v39, v35, s[6:7]
	v_lshlrev_b32_e32 v32, 3, v32
	v_lshlrev_b32_e32 v33, 3, v33
	v_lshlrev_b32_e32 v34, 3, v34
	v_lshlrev_b32_e32 v35, 3, v35
	global_load_dwordx4 v[40:43], v32, s[4:5]
	global_load_dwordx4 v[44:47], v33, s[4:5]
	global_load_dwordx4 v[48:51], v34, s[4:5]
	global_load_dwordx4 v[52:55], v35, s[4:5]
	ds_swizzle_b32 v32, v5 offset:swizzle(BITMASK_PERM, "pp100")
	ds_swizzle_b32 v33, v5 offset:swizzle(BITMASK_PERM, "pp101")
	ds_swizzle_b32 v34, v5 offset:swizzle(BITMASK_PERM, "pp110")
	ds_swizzle_b32 v35, v5 offset:swizzle(BITMASK_PERM, "pp111")
	s_waitcnt vmcnt(4)
	v_fma_mix_f32 v36, v36, 1.0, v9 op_sel_hi:[1,0,0]
	v_fma_mix_f32 v37, v37, 1.0, v9 op_sel_hi:[1,0,0]
	v_fma_mix_f32 v38, v38, 1.0, v9 op_sel_hi:[1,0,0]
	v_fma_mix_f32 v39, v39, 1.0, v9 op_sel_hi:[1,0,0]
	v_mul_f32_e32 v58, 0x3e4ccccd, v36
	v_mul_f32_e32 v59, 0x3e4ccccd, v37
	v_mul_f32_e32 v60, 0x3e4ccccd, v38
	v_mul_f32_e32 v61, 0x3e4ccccd, v39
	v_max_f32_e32 v36, v36, v58
	v_max_f32_e32 v37, v37, v59
	v_max_f32_e32 v38, v38, v60
	v_max_f32_e32 v39, v39, v61
	v_max3_f32 v56, v36, v37, v38
	v_max_f32_e32 v13, v56, v39
	v_sub_f32_e32 v36, v36, v13
	v_sub_f32_e32 v37, v37, v13
	v_sub_f32_e32 v38, v38, v13
	v_sub_f32_e32 v39, v39, v13
	v_exp_f32_e32 v36, v36
	v_exp_f32_e32 v37, v37
	v_exp_f32_e32 v38, v38
	v_exp_f32_e32 v39, v39
	s_nop 0
	v_add_f32_e32 v14, v36, v37
	v_add_f32_e32 v14, v14, v38
	v_add_f32_e32 v14, v14, v39
	s_waitcnt vmcnt(3)
	v_cvt_scalef32_pk_f16_fp8 v58, v40, 1.0
	v_cvt_scalef32_pk_f16_fp8 v59, v40, 1.0 op_sel:[1,0,0]
	v_cvt_scalef32_pk_f16_fp8 v60, v41, 1.0
	v_cvt_scalef32_pk_f16_fp8 v61, v41, 1.0 op_sel:[1,0,0]
	v_fma_mix_f32 v16, v58, v36, 0 op_sel_hi:[1,0,0]
	v_fma_mix_f32 v17, v58, v36, 0 op_sel:[1,0,0] op_sel_hi:[1,0,0]
	v_fma_mix_f32 v18, v59, v36, 0 op_sel_hi:[1,0,0]
	v_fma_mix_f32 v19, v59, v36, 0 op_sel:[1,0,0] op_sel_hi:[1,0,0]
	v_fma_mix_f32 v20, v60, v36, 0 op_sel_hi:[1,0,0]
	v_fma_mix_f32 v21, v60, v36, 0 op_sel:[1,0,0] op_sel_hi:[1,0,0]
	v_fma_mix_f32 v22, v61, v36, 0 op_sel_hi:[1,0,0]
	v_fma_mix_f32 v23, v61, v36, 0 op_sel:[1,0,0] op_sel_hi:[1,0,0]
	v_cvt_scalef32_pk_f16_fp8 v58, v42, 1.0
	v_cvt_scalef32_pk_f16_fp8 v59, v42, 1.0 op_sel:[1,0,0]
	v_cvt_scalef32_pk_f16_fp8 v60, v43, 1.0
	v_cvt_scalef32_pk_f16_fp8 v61, v43, 1.0 op_sel:[1,0,0]
	v_fma_mix_f32 v24, v58, v36, 0 op_sel_hi:[1,0,0]
	v_fma_mix_f32 v25, v58, v36, 0 op_sel:[1,0,0] op_sel_hi:[1,0,0]
	v_fma_mix_f32 v26, v59, v36, 0 op_sel_hi:[1,0,0]
	v_fma_mix_f32 v27, v59, v36, 0 op_sel:[1,0,0] op_sel_hi:[1,0,0]
	v_fma_mix_f32 v28, v60, v36, 0 op_sel_hi:[1,0,0]
	v_fma_mix_f32 v29, v60, v36, 0 op_sel:[1,0,0] op_sel_hi:[1,0,0]
	v_fma_mix_f32 v30, v61, v36, 0 op_sel_hi:[1,0,0]
	v_fma_mix_f32 v31, v61, v36, 0 op_sel:[1,0,0] op_sel_hi:[1,0,0]
	s_waitcnt vmcnt(2)
	v_cvt_scalef32_pk_f16_fp8 v58, v44, 1.0
	v_cvt_scalef32_pk_f16_fp8 v59, v44, 1.0 op_sel:[1,0,0]
	v_cvt_scalef32_pk_f16_fp8 v60, v45, 1.0
	v_cvt_scalef32_pk_f16_fp8 v61, v45, 1.0 op_sel:[1,0,0]
	v_fma_mix_f32 v16, v58, v37, v16 op_sel_hi:[1,0,0]
	v_fma_mix_f32 v17, v58, v37, v17 op_sel:[1,0,0] op_sel_hi:[1,0,0]
	v_fma_mix_f32 v18, v59, v37, v18 op_sel_hi:[1,0,0]
	v_fma_mix_f32 v19, v59, v37, v19 op_sel:[1,0,0] op_sel_hi:[1,0,0]
	v_fma_mix_f32 v20, v60, v37, v20 op_sel_hi:[1,0,0]
	v_fma_mix_f32 v21, v60, v37, v21 op_sel:[1,0,0] op_sel_hi:[1,0,0]
	v_fma_mix_f32 v22, v61, v37, v22 op_sel_hi:[1,0,0]
	v_fma_mix_f32 v23, v61, v37, v23 op_sel:[1,0,0] op_sel_hi:[1,0,0]
	v_cvt_scalef32_pk_f16_fp8 v58, v46, 1.0
	v_cvt_scalef32_pk_f16_fp8 v59, v46, 1.0 op_sel:[1,0,0]
	v_cvt_scalef32_pk_f16_fp8 v60, v47, 1.0
	v_cvt_scalef32_pk_f16_fp8 v61, v47, 1.0 op_sel:[1,0,0]
	v_fma_mix_f32 v24, v58, v37, v24 op_sel_hi:[1,0,0]
	v_fma_mix_f32 v25, v58, v37, v25 op_sel:[1,0,0] op_sel_hi:[1,0,0]
	v_fma_mix_f32 v26, v59, v37, v26 op_sel_hi:[1,0,0]
	v_fma_mix_f32 v27, v59, v37, v27 op_sel:[1,0,0] op_sel_hi:[1,0,0]
	v_fma_mix_f32 v28, v60, v37, v28 op_sel_hi:[1,0,0]
	v_fma_mix_f32 v29, v60, v37, v29 op_sel:[1,0,0] op_sel_hi:[1,0,0]
	v_fma_mix_f32 v30, v61, v37, v30 op_sel_hi:[1,0,0]
	v_fma_mix_f32 v31, v61, v37, v31 op_sel:[1,0,0] op_sel_hi:[1,0,0]
	s_waitcnt vmcnt(1)
	v_cvt_scalef32_pk_f16_fp8 v58, v48, 1.0
	v_cvt_scalef32_pk_f16_fp8 v59, v48, 1.0 op_sel:[1,0,0]
	v_cvt_scalef32_pk_f16_fp8 v60, v49, 1.0
	v_cvt_scalef32_pk_f16_fp8 v61, v49, 1.0 op_sel:[1,0,0]
	v_fma_mix_f32 v16, v58, v38, v16 op_sel_hi:[1,0,0]
	v_fma_mix_f32 v17, v58, v38, v17 op_sel:[1,0,0] op_sel_hi:[1,0,0]
	v_fma_mix_f32 v18, v59, v38, v18 op_sel_hi:[1,0,0]
	v_fma_mix_f32 v19, v59, v38, v19 op_sel:[1,0,0] op_sel_hi:[1,0,0]
	v_fma_mix_f32 v20, v60, v38, v20 op_sel_hi:[1,0,0]
	v_fma_mix_f32 v21, v60, v38, v21 op_sel:[1,0,0] op_sel_hi:[1,0,0]
	v_fma_mix_f32 v22, v61, v38, v22 op_sel_hi:[1,0,0]
	v_fma_mix_f32 v23, v61, v38, v23 op_sel:[1,0,0] op_sel_hi:[1,0,0]
	v_cvt_scalef32_pk_f16_fp8 v58, v50, 1.0
	v_cvt_scalef32_pk_f16_fp8 v59, v50, 1.0 op_sel:[1,0,0]
	v_cvt_scalef32_pk_f16_fp8 v60, v51, 1.0
	v_cvt_scalef32_pk_f16_fp8 v61, v51, 1.0 op_sel:[1,0,0]
	v_fma_mix_f32 v24, v58, v38, v24 op_sel_hi:[1,0,0]
	v_fma_mix_f32 v25, v58, v38, v25 op_sel:[1,0,0] op_sel_hi:[1,0,0]
	v_fma_mix_f32 v26, v59, v38, v26 op_sel_hi:[1,0,0]
	v_fma_mix_f32 v27, v59, v38, v27 op_sel:[1,0,0] op_sel_hi:[1,0,0]
	v_fma_mix_f32 v28, v60, v38, v28 op_sel_hi:[1,0,0]
	v_fma_mix_f32 v29, v60, v38, v29 op_sel:[1,0,0] op_sel_hi:[1,0,0]
	v_fma_mix_f32 v30, v61, v38, v30 op_sel_hi:[1,0,0]
	v_fma_mix_f32 v31, v61, v38, v31 op_sel:[1,0,0] op_sel_hi:[1,0,0]
	s_waitcnt vmcnt(0)
	v_cvt_scalef32_pk_f16_fp8 v58, v52, 1.0
	v_cvt_scalef32_pk_f16_fp8 v59, v52, 1.0 op_sel:[1,0,0]
	v_cvt_scalef32_pk_f16_fp8 v60, v53, 1.0
	v_cvt_scalef32_pk_f16_fp8 v61, v53, 1.0 op_sel:[1,0,0]
	v_fma_mix_f32 v16, v58, v39, v16 op_sel_hi:[1,0,0]
	v_fma_mix_f32 v17, v58, v39, v17 op_sel:[1,0,0] op_sel_hi:[1,0,0]
	v_fma_mix_f32 v18, v59, v39, v18 op_sel_hi:[1,0,0]
	v_fma_mix_f32 v19, v59, v39, v19 op_sel:[1,0,0] op_sel_hi:[1,0,0]
	v_fma_mix_f32 v20, v60, v39, v20 op_sel_hi:[1,0,0]
	v_fma_mix_f32 v21, v60, v39, v21 op_sel:[1,0,0] op_sel_hi:[1,0,0]
	v_fma_mix_f32 v22, v61, v39, v22 op_sel_hi:[1,0,0]
	v_fma_mix_f32 v23, v61, v39, v23 op_sel:[1,0,0] op_sel_hi:[1,0,0]
	v_cvt_scalef32_pk_f16_fp8 v58, v54, 1.0
	v_cvt_scalef32_pk_f16_fp8 v59, v54, 1.0 op_sel:[1,0,0]
	v_cvt_scalef32_pk_f16_fp8 v60, v55, 1.0
	v_cvt_scalef32_pk_f16_fp8 v61, v55, 1.0 op_sel:[1,0,0]
	v_fma_mix_f32 v24, v58, v39, v24 op_sel_hi:[1,0,0]
	v_fma_mix_f32 v25, v58, v39, v25 op_sel:[1,0,0] op_sel_hi:[1,0,0]
	v_fma_mix_f32 v26, v59, v39, v26 op_sel_hi:[1,0,0]
	v_fma_mix_f32 v27, v59, v39, v27 op_sel:[1,0,0] op_sel_hi:[1,0,0]
	v_fma_mix_f32 v28, v60, v39, v28 op_sel_hi:[1,0,0]
	v_fma_mix_f32 v29, v60, v39, v29 op_sel:[1,0,0] op_sel_hi:[1,0,0]
	v_fma_mix_f32 v30, v61, v39, v30 op_sel_hi:[1,0,0]
	v_fma_mix_f32 v31, v61, v39, v31 op_sel:[1,0,0] op_sel_hi:[1,0,0]
	s_sub_i32 s29, s29, 4
	s_branch .Lagg_B
